# attention latent loop: K/V key tiles staged by LDS-DMA (global_load_lds_dwordx4, swizzle applied on the source addresses) instead of global_load + ds_write_b128; K tile j+2 and V tile j+1 issued per s
# speedup vs baseline: 1.0143x; 1.0028x over previous
.LBB0_786:
	v_and_b32_e32 v34, 63, v171
	s_lshl_b32 s16, s0, 8
	v_and_b32_e32 v35, 0x3fffffc0, v172
	v_readlane_b32 s0, v254, 42
	v_lshlrev_b32_e32 v36, 4, v34
	v_and_b32_e32 v36, 0xc0, v36
	v_lshl_add_u32 v177, v35, 2, s0
	v_lshlrev_b32_e32 v35, 3, v34
	v_lshlrev_b32_e32 v37, 1, v34
	v_and_or_b32 v36, v35, 24, v36
	v_and_b32_e32 v37, 32, v37
	v_and_b32_e32 v35, 0x100, v35
	v_or3_b32 v192, v36, v37, v35
	s_add_i32 s1, 0, 0x400
	v_add_u32_e32 v194, s1, v192
	s_add_i32 s1, 0, 0x10400
	s_waitcnt vmcnt(4)
	s_waitcnt vmcnt(7)
	ds_write_b128 v32, v[16:19] offset:17408
	s_waitcnt vmcnt(6)
	ds_write_b128 v33, v[20:23] offset:17408
	v_add_u32_e32 v16, s1, v182
	v_exp_f32_e32 v159, v0
	v_exp_f32_e32 v161, v1
	v_exp_f32_e32 v157, v2
	v_exp_f32_e32 v160, v3
	v_exp_f32_e32 v155, v4
	v_exp_f32_e32 v158, v5
	v_exp_f32_e32 v154, v6
	v_exp_f32_e32 v156, v7
	v_exp_f32_e32 v151, v8
	v_exp_f32_e32 v153, v9
	v_exp_f32_e32 v149, v10
	v_exp_f32_e32 v152, v11
	v_exp_f32_e32 v147, v12
	v_exp_f32_e32 v150, v13
	v_exp_f32_e32 v146, v14
	v_exp_f32_e32 v148, v15
	s_waitcnt vmcnt(5)
	ds_write_b128 v16, v[24:27]
	v_add_u32_e32 v16, s1, v183
	v_mov_b32_e32 v14, v113
	v_mov_b32_e32 v15, v113
	s_waitcnt vmcnt(4)
	ds_write_b128 v16, v[28:31]
	v_cmp_gt_u32_e64 s[38:39], 32, v34
	v_mov_b32_e32 v0, v113
	v_mov_b32_e32 v1, v113
	v_mov_b32_e32 v2, v113
	v_mov_b32_e32 v3, v113
	v_mov_b32_e32 v4, v113
	v_mov_b32_e32 v5, v113
	v_mov_b32_e32 v6, v113
	v_mov_b32_e32 v7, v113
	v_mov_b32_e32 v8, v113
	v_mov_b32_e32 v9, v113
	v_mov_b32_e32 v10, v113
	v_mov_b32_e32 v11, v113
	v_mov_b32_e32 v12, v113
	v_mov_b32_e32 v13, v113
	v_mov_b64_e32 v[62:63], v[14:15]
	v_mov_b64_e32 v[46:47], v[14:15]
	v_mov_b64_e32 v[30:31], v[14:15]
	s_add_i32 s16, s16, 0x8000
	s_mov_b32 s19, 2
	s_mov_b32 s28, 4
	s_mov_b32 s0, 1
	v_lshl_add_u32 v178, v173, 2, v177
	s_mov_b32 s29, 0
	v_mov_b32_e32 v179, 0
	v_mov_b64_e32 v[60:61], v[12:13]
	v_mov_b64_e32 v[58:59], v[10:11]
	v_mov_b64_e32 v[56:57], v[8:9]
	v_mov_b64_e32 v[54:55], v[6:7]
	v_mov_b64_e32 v[52:53], v[4:5]
	v_mov_b64_e32 v[50:51], v[2:3]
	v_mov_b64_e32 v[48:49], v[0:1]
	v_mov_b64_e32 v[44:45], v[12:13]
	v_mov_b64_e32 v[42:43], v[10:11]
	v_mov_b64_e32 v[40:41], v[8:9]
	v_mov_b64_e32 v[38:39], v[6:7]
	v_mov_b64_e32 v[36:37], v[4:5]
	v_mov_b64_e32 v[34:35], v[2:3]
	v_mov_b64_e32 v[32:33], v[0:1]
	v_mov_b64_e32 v[28:29], v[12:13]
	v_mov_b64_e32 v[26:27], v[10:11]
	v_mov_b64_e32 v[24:25], v[8:9]
	v_mov_b64_e32 v[22:23], v[6:7]
	v_mov_b64_e32 v[20:21], v[4:5]
	v_mov_b64_e32 v[18:19], v[2:3]
	v_mov_b64_e32 v[16:17], v[0:1]
	s_waitcnt lgkmcnt(0)
	s_add_u32 s78, s8, s96
	s_addc_u32 s79, s9, 0
	s_add_u32 s80, s6, s96
	s_addc_u32 s81, s7, 0
	v_and_b32_e32 v183, 7, v181
	v_lshrrev_b32_e32 v185, 4, v181
	v_lshlrev_b32_e32 v185, 3, v185
	v_xor_b32_e32 v183, v183, v185
	v_and_b32_e32 v185, 15, v172
	v_xor_b32_e32 v183, v183, v185
	v_lshlrev_b32_e32 v183, 4, v183
	v_mad_u32_u24 v183, v181, s62, v183
	v_lshrrev_b32_e32 v185, 7, v172
	v_lshlrev_b32_e32 v185, 3, v185
	v_bfe_u32 v184, v172, 2, 3
	v_add_u32_e32 v185, v185, v184
	v_bfe_u32 v184, v172, 5, 2
	v_lshlrev_b32_e32 v184, 2, v184
	v_and_b32_e32 v182, 3, v172
	v_add_u32_e32 v184, v184, v182
	v_lshlrev_b32_e32 v184, 4, v184
	v_mad_u32_u24 v185, v185, s62, v184
	s_lshl_b32 s84, s90, 10
	s_add_i32 s65, s18, 0x80
	s_mul_i32 s65, s65, 0x1800
	s_add_u32 s66, s80, s65
	s_addc_u32 s67, s81, 0
	s_add_u32 s68, s66, 0x30000
	s_addc_u32 s69, s67, 0
	s_add_i32 s85, s84, 0x14400
	s_mov_b32 m0, s85
	s_nop 0
	global_load_lds_dwordx4 v183, s[66:67]
	s_add_i32 m0, s85, 0x2000
	s_nop 0
	global_load_lds_dwordx4 v183, s[68:69]
	s_barrier
.LBB0_787:
	s_mov_b32 s54, s0
	s_add_i32 s55, s28, -3
	s_lshl_b32 s21, s0, 14
	v_add_u32_e32 v180, s21, v191
	v_add_u32_e32 v84, v180, v190
	ds_read_b128 v[80:83], v84 offset:50176
	ds_read_b128 v[84:87], v84 offset:58368
	v_add_u32_e32 v195, v180, v188
	ds_read_b128 v[196:199], v195 offset:50176
	ds_read_b128 v[200:203], v195 offset:58368
	v_add_u32_e32 v195, v180, v187
	s_waitcnt lgkmcnt(3)
	v_mfma_f32_32x32x16_bf16 v[96:111], v[80:83], v[122:125], 0
	v_add_u32_e32 v180, v180, v186
	v_exp_f32_e32 v204, v72
	v_exp_f32_e32 v205, v73
	v_exp_f32_e32 v206, v74
	v_exp_f32_e32 v207, v75
	v_exp_f32_e32 v208, v76
	v_exp_f32_e32 v209, v77
	s_waitcnt lgkmcnt(2)
	v_mfma_f32_32x32x16_bf16 v[80:95], v[84:87], v[122:125], 0
	v_exp_f32_e32 v210, v78
	v_exp_f32_e32 v79, v79
	s_waitcnt lgkmcnt(1)
	v_mfma_f32_32x32x16_bf16 v[96:111], v[196:199], v[126:129], v[96:111]
	s_waitcnt lgkmcnt(0)
	v_mfma_f32_32x32x16_bf16 v[80:95], v[200:203], v[126:129], v[80:95]
	ds_read_b128 v[196:199], v195 offset:50176
	ds_read_b128 v[200:203], v195 offset:58368
	s_waitcnt lgkmcnt(1)
	v_mfma_f32_32x32x16_bf16 v[96:111], v[196:199], v[118:121], v[96:111]
	s_waitcnt lgkmcnt(0)
	v_mfma_f32_32x32x16_bf16 v[80:95], v[200:203], v[118:121], v[80:95]
	ds_read_b128 v[196:199], v180 offset:50176
	ds_read_b128 v[200:203], v180 offset:58368
	v_exp_f32_e32 v180, v64
	v_add_f32_e32 v64, v161, v159
	v_add_f32_e32 v195, v157, v160
	v_add_f32_e32 v64, v155, v64
	v_add_f32_e32 v195, v158, v195
	v_add_f32_e32 v64, v154, v64
	v_add_f32_e32 v195, v156, v195
	v_add_f32_e32 v64, v151, v64
	v_add_f32_e32 v195, v153, v195
	v_add_f32_e32 v64, v149, v64
	v_add_f32_e32 v195, v152, v195
	v_add_f32_e32 v64, v147, v64
	s_waitcnt lgkmcnt(1)
	v_mfma_f32_32x32x16_bf16 v[96:111], v[196:199], v[114:117], v[96:111]
	v_exp_f32_e32 v197, v65
	v_add_f32_e32 v195, v150, v195
	v_exp_f32_e32 v198, v66
	v_add_f32_e32 v64, v146, v64
	v_exp_f32_e32 v199, v67
	v_add_f32_e32 v195, v148, v195
	v_add_f32_e32 v64, v180, v64
	s_waitcnt lgkmcnt(0)
	v_mfma_f32_32x32x16_bf16 v[80:95], v[200:203], v[114:117], v[80:95]
	v_exp_f32_e32 v200, v68
	v_exp_f32_e32 v201, v69
	v_add_f32_e32 v195, v197, v195
	v_exp_f32_e32 v202, v70
	v_add_f32_e32 v64, v198, v64
	v_exp_f32_e32 v203, v71
	v_add_f32_e32 v195, v199, v195
	v_add_f32_e32 v64, v200, v64
	v_add_f32_e32 v195, v201, v195
	v_add_f32_e32 v64, v202, v64
	v_add_f32_e32 v195, v203, v195
	v_add_f32_e32 v64, v204, v64
	v_add_f32_e32 v195, v205, v195
	v_add_f32_e32 v64, v206, v64
	v_add_f32_e32 v195, v207, v195
	v_add_f32_e32 v64, v208, v64
	v_add_f32_e32 v195, v209, v195
	v_add_f32_e32 v64, v210, v64
	v_add_f32_e32 v195, v79, v195
	v_add_f32_e32 v195, v195, v64
	v_cvt_pk_bf16_f32 v64, v159, v161
	v_cvt_pk_bf16_f32 v65, v157, v160
	v_cvt_pk_bf16_f32 v66, v155, v158
	v_cvt_pk_bf16_f32 v67, v154, v156
	v_cvt_pk_bf16_f32 v68, v151, v153
	v_cvt_pk_bf16_f32 v69, v149, v152
	v_cvt_pk_bf16_f32 v70, v147, v150
	v_cvt_pk_bf16_f32 v71, v146, v148
	v_cvt_pk_bf16_f32 v72, v180, v197
	v_cvt_pk_bf16_f32 v73, v198, v199
	v_cvt_pk_bf16_f32 v74, v200, v201
	v_cvt_pk_bf16_f32 v75, v202, v203
	v_cvt_pk_bf16_f32 v76, v204, v205
	v_cvt_pk_bf16_f32 v77, v206, v207
	v_cvt_pk_bf16_f32 v78, v208, v209
	v_cvt_pk_bf16_f32 v79, v210, v79
	s_cmp_lt_u32 s55, 30
	s_cselect_b32 s0, 0, 0xffffffe0
	s_cselect_b32 s1, s18, s16
	s_add_i32 s0, s0, s28
	s_lshl_b32 s0, s0, 6
	s_add_i32 s0, s0, s1
	s_sub_i32 s0, s0, 64
	s_mul_i32 s64, s0, 0x1800
	s_add_u32 s66, s78, s65
	s_addc_u32 s67, s79, 0
	s_add_u32 s68, s66, 0x30000
	s_addc_u32 s69, s67, 0
	s_add_u32 s70, s80, s64
	s_addc_u32 s71, s81, 0
	s_add_u32 s72, s70, 0x30000
	s_addc_u32 s73, s71, 0
	s_lshl_b32 s85, s29, 14
	s_add_i32 s85, s85, s84
	s_add_i32 m0, s85, 0xc400
	s_nop 0
	global_load_lds_dwordx4 v183, s[70:71]
	s_add_i32 m0, s85, 0xe400
	s_nop 0
	global_load_lds_dwordx4 v183, s[72:73]
	s_lshl_b32 s85, s19, 14
	s_add_i32 s85, s85, s84
	s_add_i32 m0, s85, 0x400
	s_nop 0
	global_load_lds_dwordx4 v185, s[66:67]
	s_add_i32 m0, s85, 0x2400
	s_nop 0
	global_load_lds_dwordx4 v185, s[68:69]
	s_mov_b32 s65, s64
	s_lshl_b32 s20, s29, 14
	v_add_u32_e32 v180, s20, v194
	ds_read_b64_tr_b16 v[198:199], v180 offset:0
	ds_read_b64_tr_b16 v[200:201], v180 offset:0x800
	ds_read_b64_tr_b16 v[202:203], v180 offset:0x1000
	ds_read_b64_tr_b16 v[204:205], v180 offset:0x1800
	ds_read_b64_tr_b16 v[206:207], v180 offset:0x2000
	ds_read_b64_tr_b16 v[208:209], v180 offset:0x2800
	ds_read_b64_tr_b16 v[222:223], v180 offset:0x3000
	ds_read_b64_tr_b16 v[224:225], v180 offset:0x3800
	s_waitcnt lgkmcnt(0)
	s_nop 0
	v_mfma_f32_32x32x16_bf16 v[0:15], v[64:67], v[198:201], v[0:15]
	ds_read_b64_tr_b16 v[198:199], v180 offset:0x200
	ds_read_b64_tr_b16 v[200:201], v180 offset:0xa00
	v_mfma_f32_32x32x16_bf16 v[0:15], v[68:71], v[202:205], v[0:15]
	ds_read_b64_tr_b16 v[202:203], v180 offset:0x1200
	ds_read_b64_tr_b16 v[204:205], v180 offset:0x1a00
	v_mfma_f32_32x32x16_bf16 v[0:15], v[72:75], v[206:209], v[0:15]
	ds_read_b64_tr_b16 v[206:207], v180 offset:0x2200
	ds_read_b64_tr_b16 v[208:209], v180 offset:0x2a00
	v_mfma_f32_32x32x16_bf16 v[0:15], v[76:79], v[222:225], v[0:15]
	ds_read_b64_tr_b16 v[222:223], v180 offset:0x3200
	ds_read_b64_tr_b16 v[224:225], v180 offset:0x3a00
	s_waitcnt lgkmcnt(0)
	v_mfma_f32_32x32x16_bf16 v[48:63], v[64:67], v[198:201], v[48:63]
	ds_read_b64_tr_b16 v[198:199], v180 offset:0x400
	ds_read_b64_tr_b16 v[200:201], v180 offset:0xc00
	v_mfma_f32_32x32x16_bf16 v[48:63], v[68:71], v[202:205], v[48:63]
	ds_read_b64_tr_b16 v[202:203], v180 offset:0x1400
	ds_read_b64_tr_b16 v[204:205], v180 offset:0x1c00
	v_mfma_f32_32x32x16_bf16 v[48:63], v[72:75], v[206:209], v[48:63]
	ds_read_b64_tr_b16 v[206:207], v180 offset:0x2400
	ds_read_b64_tr_b16 v[208:209], v180 offset:0x2c00
	v_mfma_f32_32x32x16_bf16 v[48:63], v[76:79], v[222:225], v[48:63]
	ds_read_b64_tr_b16 v[222:223], v180 offset:0x3400
	ds_read_b64_tr_b16 v[224:225], v180 offset:0x3c00
	s_waitcnt lgkmcnt(0)
	v_mfma_f32_32x32x16_bf16 v[32:47], v[64:67], v[198:201], v[32:47]
	ds_read_b64_tr_b16 v[198:199], v180 offset:0x600
	ds_read_b64_tr_b16 v[200:201], v180 offset:0xe00
	v_mfma_f32_32x32x16_bf16 v[32:47], v[68:71], v[202:205], v[32:47]
	ds_read_b64_tr_b16 v[202:203], v180 offset:0x1600
	ds_read_b64_tr_b16 v[204:205], v180 offset:0x1e00
	v_mfma_f32_32x32x16_bf16 v[32:47], v[72:75], v[206:209], v[32:47]
	ds_read_b64_tr_b16 v[206:207], v180 offset:0x2600
	ds_read_b64_tr_b16 v[208:209], v180 offset:0x2e00
	v_mfma_f32_32x32x16_bf16 v[32:47], v[76:79], v[222:225], v[32:47]
	ds_read_b64_tr_b16 v[222:223], v180 offset:0x3600
	ds_read_b64_tr_b16 v[224:225], v180 offset:0x3e00
	s_waitcnt lgkmcnt(0)
	v_mfma_f32_32x32x16_bf16 v[16:31], v[64:67], v[198:201], v[16:31]
	v_max_f32_e32 v64, v96, v97
	v_max3_f32 v65, v80, v81, v82
	v_max3_f32 v64, v64, v98, v99
	v_max3_f32 v65, v65, v83, v84
	v_max3_f32 v64, v64, v100, v101
	v_mfma_f32_32x32x16_bf16 v[16:31], v[68:71], v[202:205], v[16:31]
	v_max3_f32 v65, v65, v85, v86
	v_max3_f32 v64, v64, v102, v103
	v_max3_f32 v65, v65, v87, v88
	v_max3_f32 v64, v64, v104, v105
	v_max3_f32 v65, v65, v89, v90
	v_max3_f32 v64, v64, v106, v107
	v_max3_f32 v65, v65, v91, v92
	v_mfma_f32_32x32x16_bf16 v[16:31], v[72:75], v[206:209], v[16:31]
	v_max3_f32 v64, v64, v108, v109
	v_max3_f32 v65, v65, v93, v94
	v_max3_f32 v64, v64, v110, v111
	v_max3_f32 v64, v64, v65, v95
	v_mov_b32_e32 v198, 1.0
	v_mfma_f32_32x32x16_bf16 v[16:31], v[76:79], v[222:225], v[16:31]
	v_cmp_ge_f32_e64 s[40:41], s75, v64
	s_and_b64 s[0:1], s[56:57], s[40:41]
	s_cmp_eq_u64 s[0:1], exec
	s_cbranch_scc0 .LBB0_801
.LBB0_788:
	s_lshl_b32 s0, s19, 14
	s_add_i32 s22, s0, 0
	v_cmp_gt_f32_e32 vcc, 1.0, v198
	s_cbranch_vccz .LBB0_792
	s_and_saveexec_b64 s[0:1], s[38:39]
	ds_write_b32 v178, v198 offset:128
	s_or_b64 exec, exec, s[0:1]
	s_waitcnt lgkmcnt(0)
	v_add_u32_e32 v76, v177, v112
	ds_read_b128 v[64:67], v76 offset:224
	ds_read_b128 v[68:71], v76 offset:192
	ds_read_b128 v[72:75], v76 offset:160
	ds_read_b128 v[76:79], v76 offset:128
	s_waitcnt lgkmcnt(3)
	v_pk_mul_f32 v[12:13], v[12:13], v[64:65]
	s_waitcnt lgkmcnt(2)
	v_pk_mul_f32 v[8:9], v[8:9], v[68:69]
	s_waitcnt lgkmcnt(1)
	v_pk_mul_f32 v[4:5], v[4:5], v[72:73]
	v_pk_mul_f32 v[14:15], v[14:15], v[66:67]
	v_pk_mul_f32 v[10:11], v[10:11], v[70:71]
	v_pk_mul_f32 v[6:7], v[6:7], v[74:75]
	s_waitcnt lgkmcnt(0)
	v_pk_mul_f32 v[2:3], v[2:3], v[78:79]
	v_pk_mul_f32 v[0:1], v[0:1], v[76:77]
	v_pk_mul_f32 v[60:61], v[60:61], v[64:65]
	v_pk_mul_f32 v[56:57], v[56:57], v[68:69]
	v_pk_mul_f32 v[52:53], v[52:53], v[72:73]
	v_pk_mul_f32 v[62:63], v[62:63], v[66:67]
	v_pk_mul_f32 v[58:59], v[58:59], v[70:71]
	v_pk_mul_f32 v[54:55], v[54:55], v[74:75]
	v_pk_mul_f32 v[50:51], v[50:51], v[78:79]
	v_pk_mul_f32 v[48:49], v[48:49], v[76:77]
	v_pk_mul_f32 v[44:45], v[44:45], v[64:65]
	v_pk_mul_f32 v[40:41], v[40:41], v[68:69]
	v_pk_mul_f32 v[36:37], v[36:37], v[72:73]
	v_pk_mul_f32 v[46:47], v[46:47], v[66:67]
	v_pk_mul_f32 v[42:43], v[42:43], v[70:71]
	v_pk_mul_f32 v[38:39], v[38:39], v[74:75]
	v_pk_mul_f32 v[34:35], v[34:35], v[78:79]
	v_pk_mul_f32 v[32:33], v[32:33], v[76:77]
	v_pk_mul_f32 v[28:29], v[28:29], v[64:65]
	v_pk_mul_f32 v[24:25], v[24:25], v[68:69]
	v_pk_mul_f32 v[20:21], v[20:21], v[72:73]
	v_pk_mul_f32 v[30:31], v[30:31], v[66:67]
	v_pk_mul_f32 v[26:27], v[26:27], v[70:71]
	v_pk_mul_f32 v[22:23], v[22:23], v[74:75]
	v_pk_mul_f32 v[18:19], v[18:19], v[78:79]
	v_pk_mul_f32 v[16:17], v[16:17], v[76:77]
.LBB0_792:
	v_exp_f32_e32 v197, v96
	v_exp_f32_e32 v208, v97
	v_exp_f32_e32 v209, v98
	v_exp_f32_e32 v210, v99
	v_exp_f32_e32 v211, v100
	v_exp_f32_e32 v220, v101
	v_exp_f32_e32 v221, v102
	v_exp_f32_e32 v222, v103
	v_exp_f32_e32 v223, v104
	v_exp_f32_e32 v224, v105
	v_exp_f32_e32 v225, v106
	v_exp_f32_e32 v226, v107
	v_exp_f32_e32 v227, v108
	v_exp_f32_e32 v228, v109
	v_exp_f32_e32 v229, v110
	v_exp_f32_e32 v230, v111
	s_waitcnt lgkmcnt(0)
	s_waitcnt vmcnt(4)
	s_barrier
	v_add_u32_e32 v199, s22, v189
	v_add_u32_e32 v68, v199, v190
	ds_read_b128 v[64:67], v68 offset:50176
	ds_read_b128 v[68:71], v68 offset:58368
	v_add_u32_e32 v204, v199, v188
	ds_read_b128 v[200:203], v204 offset:50176
	ds_read_b128 v[204:207], v204 offset:58368
	v_exp_f32_e32 v231, v87
	s_waitcnt lgkmcnt(3)
	v_mfma_f32_32x32x16_bf16 v[96:111], v[64:67], v[122:125], 0
	v_exp_f32_e32 v232, v88
	v_exp_f32_e32 v233, v89
	v_exp_f32_e32 v234, v90
	v_exp_f32_e32 v235, v91
	v_exp_f32_e32 v236, v92
	v_exp_f32_e32 v237, v93
	v_exp_f32_e32 v238, v94
	s_waitcnt lgkmcnt(2)
	v_mfma_f32_32x32x16_bf16 v[64:79], v[68:71], v[122:125], 0
	v_exp_f32_e32 v95, v95
	s_waitcnt lgkmcnt(1)
	v_mfma_f32_32x32x16_bf16 v[96:111], v[200:203], v[126:129], v[96:111]
	s_waitcnt lgkmcnt(0)
	v_mfma_f32_32x32x16_bf16 v[64:79], v[204:207], v[126:129], v[64:79]
	v_add_u32_e32 v204, v199, v187
	ds_read_b128 v[200:203], v204 offset:50176
	ds_read_b128 v[204:207], v204 offset:58368
	v_add_u32_e32 v199, v199, v186
	s_waitcnt lgkmcnt(1)
	v_mfma_f32_32x32x16_bf16 v[96:111], v[200:203], v[118:121], v[96:111]
	s_waitcnt lgkmcnt(0)
	v_mfma_f32_32x32x16_bf16 v[64:79], v[204:207], v[118:121], v[64:79]
	ds_read_b128 v[200:203], v199 offset:50176
	ds_read_b128 v[204:207], v199 offset:58368
	s_waitcnt lgkmcnt(1)
	v_mfma_f32_32x32x16_bf16 v[96:111], v[200:203], v[114:117], v[96:111]
	v_exp_f32_e32 v201, v80
	v_add_f32_e32 v80, v208, v197
	v_add_f32_e32 v199, v209, v210
	v_add_f32_e32 v80, v211, v80
	v_add_f32_e32 v199, v220, v199
	v_add_f32_e32 v80, v221, v80
	v_add_f32_e32 v199, v222, v199
	v_add_f32_e32 v80, v223, v80
	v_add_f32_e32 v199, v224, v199
	v_add_f32_e32 v80, v225, v80
	v_add_f32_e32 v199, v226, v199
	v_add_f32_e32 v80, v227, v80
	v_exp_f32_e32 v202, v81
	v_add_f32_e32 v199, v228, v199
	v_exp_f32_e32 v203, v82
	v_add_f32_e32 v80, v229, v80
	s_waitcnt lgkmcnt(0)
	v_mfma_f32_32x32x16_bf16 v[64:79], v[204:207], v[114:117], v[64:79]
	v_exp_f32_e32 v204, v83
	v_add_f32_e32 v199, v230, v199
	v_exp_f32_e32 v205, v84
	v_add_f32_e32 v80, v201, v80
	v_exp_f32_e32 v206, v85
	v_add_f32_e32 v199, v202, v199
	v_exp_f32_e32 v207, v86
	v_add_f32_e32 v80, v203, v80
	v_add_f32_e32 v199, v204, v199
	v_add_f32_e32 v80, v205, v80
	v_add_f32_e32 v199, v206, v199
	v_add_f32_e32 v80, v207, v80
	v_add_f32_e32 v199, v231, v199
	v_add_f32_e32 v80, v232, v80
	v_add_f32_e32 v199, v233, v199
	v_add_f32_e32 v80, v234, v80
	v_add_f32_e32 v199, v235, v199
	v_add_f32_e32 v80, v236, v80
	v_add_f32_e32 v199, v237, v199
	v_add_f32_e32 v80, v238, v80
	v_add_f32_e32 v199, v95, v199
	v_add_f32_e32 v199, v199, v80
	v_cvt_pk_bf16_f32 v80, v197, v208
	v_cvt_pk_bf16_f32 v81, v209, v210
	v_cvt_pk_bf16_f32 v82, v211, v220
	v_cvt_pk_bf16_f32 v83, v221, v222
	v_cvt_pk_bf16_f32 v84, v223, v224
	v_cvt_pk_bf16_f32 v85, v225, v226
	v_cvt_pk_bf16_f32 v86, v227, v228
	v_cvt_pk_bf16_f32 v87, v229, v230
	v_cvt_pk_bf16_f32 v88, v201, v202
	v_cvt_pk_bf16_f32 v89, v203, v204
	v_cvt_pk_bf16_f32 v90, v205, v206
	v_cvt_pk_bf16_f32 v91, v207, v231
	v_cvt_pk_bf16_f32 v92, v232, v233
	v_cvt_pk_bf16_f32 v93, v234, v235
	v_cvt_pk_bf16_f32 v94, v236, v237
	v_cvt_pk_bf16_f32 v95, v238, v95
	s_cmp_lt_u32 s55, 29
	s_cselect_b32 s0, 0, 0xffffffe0
	s_cselect_b32 s1, s18, s16
	s_add_i32 s0, s0, s28
	s_lshl_b32 s0, s0, 6
	s_add_i32 s0, s0, s1
	s_mul_i32 s64, s0, 0x1800
	s_add_u32 s66, s78, s65
	s_addc_u32 s67, s79, 0
	s_add_u32 s68, s66, 0x30000
	s_addc_u32 s69, s67, 0
	s_add_u32 s70, s80, s64
	s_addc_u32 s71, s81, 0
	s_add_u32 s72, s70, 0x30000
	s_addc_u32 s73, s71, 0
	s_lshl_b32 s85, s54, 14
	s_add_i32 s85, s85, s84
	s_add_i32 m0, s85, 0xc400
	s_nop 0
	global_load_lds_dwordx4 v183, s[70:71]
	s_add_i32 m0, s85, 0xe400
	s_nop 0
	global_load_lds_dwordx4 v183, s[72:73]
	s_lshl_b32 s85, s29, 14
	s_add_i32 s85, s85, s84
	s_add_i32 m0, s85, 0x400
	s_nop 0
	global_load_lds_dwordx4 v185, s[66:67]
	s_add_i32 m0, s85, 0x2400
	s_nop 0
	global_load_lds_dwordx4 v185, s[68:69]
	s_mov_b32 s65, s64

.LBB0_795:
	s_add_i32 s20, s20, 0
	v_cmp_gt_f32_e32 vcc, 1.0, v197
	s_cbranch_vccz .LBB0_799
	s_and_saveexec_b64 s[0:1], s[38:39]
	ds_write_b32 v178, v197 offset:128
	s_or_b64 exec, exec, s[0:1]
	s_waitcnt lgkmcnt(0)
	v_add_u32_e32 v92, v177, v112
	ds_read_b128 v[80:83], v92 offset:224
	ds_read_b128 v[84:87], v92 offset:192
	ds_read_b128 v[88:91], v92 offset:160
	ds_read_b128 v[92:95], v92 offset:128
	s_waitcnt lgkmcnt(3)
	v_pk_mul_f32 v[12:13], v[12:13], v[80:81]
	s_waitcnt lgkmcnt(2)
	v_pk_mul_f32 v[8:9], v[8:9], v[84:85]
	s_waitcnt lgkmcnt(1)
	v_pk_mul_f32 v[4:5], v[4:5], v[88:89]
	v_pk_mul_f32 v[14:15], v[14:15], v[82:83]
	v_pk_mul_f32 v[10:11], v[10:11], v[86:87]
	v_pk_mul_f32 v[6:7], v[6:7], v[90:91]
	s_waitcnt lgkmcnt(0)
	v_pk_mul_f32 v[2:3], v[2:3], v[94:95]
	v_pk_mul_f32 v[0:1], v[0:1], v[92:93]
	v_pk_mul_f32 v[60:61], v[60:61], v[80:81]
	v_pk_mul_f32 v[56:57], v[56:57], v[84:85]
	v_pk_mul_f32 v[52:53], v[52:53], v[88:89]
	v_pk_mul_f32 v[62:63], v[62:63], v[82:83]
	v_pk_mul_f32 v[58:59], v[58:59], v[86:87]
	v_pk_mul_f32 v[54:55], v[54:55], v[90:91]
	v_pk_mul_f32 v[50:51], v[50:51], v[94:95]
	v_pk_mul_f32 v[48:49], v[48:49], v[92:93]
	v_pk_mul_f32 v[44:45], v[44:45], v[80:81]
	v_pk_mul_f32 v[40:41], v[40:41], v[84:85]
	v_pk_mul_f32 v[36:37], v[36:37], v[88:89]
	v_pk_mul_f32 v[46:47], v[46:47], v[82:83]
	v_pk_mul_f32 v[42:43], v[42:43], v[86:87]
	v_pk_mul_f32 v[38:39], v[38:39], v[90:91]
	v_pk_mul_f32 v[34:35], v[34:35], v[94:95]
	v_pk_mul_f32 v[32:33], v[32:33], v[92:93]
	v_pk_mul_f32 v[28:29], v[28:29], v[80:81]
	v_pk_mul_f32 v[24:25], v[24:25], v[84:85]
	v_pk_mul_f32 v[20:21], v[20:21], v[88:89]
	v_pk_mul_f32 v[30:31], v[30:31], v[82:83]
	v_pk_mul_f32 v[26:27], v[26:27], v[86:87]
	v_pk_mul_f32 v[22:23], v[22:23], v[90:91]
	v_pk_mul_f32 v[18:19], v[18:19], v[94:95]
	v_pk_mul_f32 v[16:17], v[16:17], v[92:93]
.LBB0_799:
	v_exp_f32_e32 v159, v96
	v_exp_f32_e32 v161, v97
	v_exp_f32_e32 v157, v98
	v_exp_f32_e32 v160, v99
	v_exp_f32_e32 v155, v100
	v_exp_f32_e32 v158, v101
	v_exp_f32_e32 v154, v102
	v_exp_f32_e32 v156, v103
	v_exp_f32_e32 v151, v104
	v_exp_f32_e32 v153, v105
	v_exp_f32_e32 v149, v106
	v_exp_f32_e32 v152, v107
	v_exp_f32_e32 v147, v108
	v_exp_f32_e32 v150, v109
	v_exp_f32_e32 v146, v110
	v_exp_f32_e32 v148, v111
	v_fma_f32 v80, v193, v179, v195
	s_add_i32 s28, s28, 2
	v_fma_f32 v179, v80, v198, v199
	s_cmp_gt_u32 s55, 32
	s_waitcnt lgkmcnt(0)
	s_waitcnt vmcnt(4)
	s_barrier
	s_cbranch_scc1 .LBB0_803
	s_mov_b32 s0, s29
	s_mov_b32 s29, s19
	s_mov_b32 s19, s54
	v_mov_b32_e32 v193, v197
	s_branch .LBB0_787

.LBB0_803:
	s_waitcnt vmcnt(0)
	s_barrier
	v_add_u32_e32 v134, s20, v189
	v_add_u32_e32 v84, v134, v190
	ds_read_b128 v[80:83], v84 offset:50176
	ds_read_b128 v[84:87], v84 offset:58368
	v_add_u32_e32 v130, v134, v188
	v_exp_f32_e32 v78, v78
	v_exp_f32_e32 v79, v79
	s_waitcnt lgkmcnt(1)
	v_mfma_f32_32x32x16_bf16 v[96:111], v[80:83], v[122:125], 0
	s_waitcnt lgkmcnt(0)
	v_mfma_f32_32x32x16_bf16 v[80:95], v[84:87], v[122:125], 0
	ds_read_b128 v[122:125], v130 offset:50176
	ds_read_b128 v[130:133], v130 offset:58368
	s_waitcnt lgkmcnt(1)
	v_mfma_f32_32x32x16_bf16 v[96:111], v[122:125], v[126:129], v[96:111]
	s_waitcnt lgkmcnt(0)
	v_mfma_f32_32x32x16_bf16 v[80:95], v[130:133], v[126:129], v[80:95]
	v_add_u32_e32 v126, v134, v187
	ds_read_b128 v[122:125], v126 offset:50176
	ds_read_b128 v[126:129], v126 offset:58368
	s_waitcnt lgkmcnt(1)
	v_mfma_f32_32x32x16_bf16 v[96:111], v[122:125], v[118:121], v[96:111]
	v_add_u32_e32 v122, v134, v186
	s_waitcnt lgkmcnt(0)
	v_mfma_f32_32x32x16_bf16 v[80:95], v[126:129], v[118:121], v[80:95]
	ds_read_b128 v[118:121], v122 offset:50176
	ds_read_b128 v[122:125], v122 offset:58368
	v_exp_f32_e32 v126, v76
	v_exp_f32_e32 v127, v77
	s_waitcnt lgkmcnt(1)
	v_mfma_f32_32x32x16_bf16 v[96:111], v[118:121], v[114:117], v[96:111]
	v_exp_f32_e32 v118, v68
	v_exp_f32_e32 v119, v69
	v_exp_f32_e32 v120, v70
	v_exp_f32_e32 v121, v71
	s_waitcnt lgkmcnt(0)
	v_mfma_f32_32x32x16_bf16 v[80:95], v[122:125], v[114:117], v[80:95]
	v_exp_f32_e32 v114, v64
	v_add_f32_e32 v64, 0, v159
	v_add_f32_e32 v64, v161, v64
	v_add_f32_e32 v64, v157, v64
	v_add_f32_e32 v64, v160, v64
	v_add_f32_e32 v64, v155, v64
	v_add_f32_e32 v64, v158, v64
	v_add_f32_e32 v64, v154, v64
	v_add_f32_e32 v64, v156, v64
	v_add_f32_e32 v64, v151, v64
	v_add_f32_e32 v64, v153, v64
	v_add_f32_e32 v64, v149, v64
	v_add_f32_e32 v64, v152, v64
	v_add_f32_e32 v64, v147, v64
	v_exp_f32_e32 v115, v65
	v_add_f32_e32 v64, v150, v64
	v_exp_f32_e32 v116, v66
	v_add_f32_e32 v64, v146, v64
	v_exp_f32_e32 v117, v67
	v_add_f32_e32 v64, v148, v64
	v_add_f32_e32 v64, v114, v64
	v_add_f32_e32 v64, v115, v64
	v_add_f32_e32 v64, v116, v64
	v_add_f32_e32 v64, v117, v64
	v_exp_f32_e32 v122, v72
	v_add_f32_e32 v64, v118, v64
	v_exp_f32_e32 v123, v73
	v_add_f32_e32 v64, v119, v64
	v_exp_f32_e32 v124, v74
	v_add_f32_e32 v64, v120, v64
	v_exp_f32_e32 v125, v75
	v_add_f32_e32 v64, v121, v64
	v_add_f32_e32 v64, v122, v64
	v_add_f32_e32 v64, v123, v64
	v_add_f32_e32 v64, v124, v64
	v_add_f32_e32 v64, v125, v64
	v_add_f32_e32 v64, v126, v64
	v_add_f32_e32 v64, v127, v64
	v_add_f32_e32 v64, v78, v64
	v_add_f32_e32 v64, v79, v64
	v_cvt_pk_bf16_f32 v66, v159, v161
	v_cvt_pk_bf16_f32 v67, v157, v160
	v_cvt_pk_bf16_f32 v68, v155, v158
	v_cvt_pk_bf16_f32 v69, v154, v156
	v_cvt_pk_bf16_f32 v70, v151, v153
	v_cvt_pk_bf16_f32 v71, v149, v152
	v_cvt_pk_bf16_f32 v72, v147, v150
	v_cvt_pk_bf16_f32 v73, v146, v148
	v_cvt_pk_bf16_f32 v74, v114, v115
	v_cvt_pk_bf16_f32 v75, v116, v117
	v_cvt_pk_bf16_f32 v76, v118, v119
	v_cvt_pk_bf16_f32 v77, v120, v121
	v_cvt_pk_bf16_f32 v114, v122, v123
	v_cvt_pk_bf16_f32 v115, v124, v125
	v_cvt_pk_bf16_f32 v116, v126, v127
	v_cvt_pk_bf16_f32 v117, v78, v79
	s_nop 0
	s_add_i32 s0, 0, 0x4400
	v_add_u32_e32 v78, s0, v192
	ds_read_b64_tr_b16 v[118:119], v78 offset:0
	ds_read_b64_tr_b16 v[120:121], v78 offset:0x800
	ds_read_b64_tr_b16 v[122:123], v78 offset:0x1000
	ds_read_b64_tr_b16 v[124:125], v78 offset:0x1800
	ds_read_b64_tr_b16 v[126:127], v78 offset:0x2000
	ds_read_b64_tr_b16 v[128:129], v78 offset:0x2800
	ds_read_b64_tr_b16 v[130:131], v78 offset:0x3000
	ds_read_b64_tr_b16 v[132:133], v78 offset:0x3800
	s_waitcnt lgkmcnt(0)
	s_nop 0
	v_mfma_f32_32x32x16_bf16 v[0:15], v[66:69], v[118:121], v[0:15]
	ds_read_b64_tr_b16 v[118:119], v78 offset:0x200
	ds_read_b64_tr_b16 v[120:121], v78 offset:0xa00
	v_mfma_f32_32x32x16_bf16 v[0:15], v[70:73], v[122:125], v[0:15]
	ds_read_b64_tr_b16 v[122:123], v78 offset:0x1200
	ds_read_b64_tr_b16 v[124:125], v78 offset:0x1a00
	v_mfma_f32_32x32x16_bf16 v[0:15], v[74:77], v[126:129], v[0:15]
	ds_read_b64_tr_b16 v[126:127], v78 offset:0x2200
	ds_read_b64_tr_b16 v[128:129], v78 offset:0x2a00
	v_mfma_f32_32x32x16_bf16 v[0:15], v[114:117], v[130:133], v[0:15]
	ds_read_b64_tr_b16 v[130:131], v78 offset:0x3200
	ds_read_b64_tr_b16 v[132:133], v78 offset:0x3a00
	s_waitcnt lgkmcnt(0)
	v_mfma_f32_32x32x16_bf16 v[48:63], v[66:69], v[118:121], v[48:63]
	ds_read_b64_tr_b16 v[118:119], v78 offset:0x400
	ds_read_b64_tr_b16 v[120:121], v78 offset:0xc00
	v_mfma_f32_32x32x16_bf16 v[48:63], v[70:73], v[122:125], v[48:63]
	ds_read_b64_tr_b16 v[122:123], v78 offset:0x1400
	ds_read_b64_tr_b16 v[124:125], v78 offset:0x1c00
	v_mfma_f32_32x32x16_bf16 v[48:63], v[74:77], v[126:129], v[48:63]
	ds_read_b64_tr_b16 v[126:127], v78 offset:0x2400
	ds_read_b64_tr_b16 v[128:129], v78 offset:0x2c00
	v_mfma_f32_32x32x16_bf16 v[48:63], v[114:117], v[130:133], v[48:63]
	ds_read_b64_tr_b16 v[130:131], v78 offset:0x3400
	ds_read_b64_tr_b16 v[132:133], v78 offset:0x3c00
	s_waitcnt lgkmcnt(0)
	v_mfma_f32_32x32x16_bf16 v[32:47], v[66:69], v[118:121], v[32:47]
	ds_read_b64_tr_b16 v[118:119], v78 offset:0x600
	ds_read_b64_tr_b16 v[120:121], v78 offset:0xe00
	v_mfma_f32_32x32x16_bf16 v[32:47], v[70:73], v[122:125], v[32:47]
	ds_read_b64_tr_b16 v[122:123], v78 offset:0x1600
	ds_read_b64_tr_b16 v[124:125], v78 offset:0x1e00
	v_mfma_f32_32x32x16_bf16 v[32:47], v[74:77], v[126:129], v[32:47]
	ds_read_b64_tr_b16 v[126:127], v78 offset:0x2600
	ds_read_b64_tr_b16 v[128:129], v78 offset:0x2e00
	v_mfma_f32_32x32x16_bf16 v[32:47], v[114:117], v[130:133], v[32:47]
	ds_read_b64_tr_b16 v[130:131], v78 offset:0x3600
	ds_read_b64_tr_b16 v[132:133], v78 offset:0x3e00
	s_waitcnt lgkmcnt(0)
	v_mfma_f32_32x32x16_bf16 v[16:31], v[66:69], v[118:121], v[16:31]
	v_max_f32_e32 v66, v97, v97
	v_max_f32_e32 v67, v96, v96
	v_max_f32_e32 v66, v67, v66
	v_max3_f32 v66, v66, v98, v99
	v_max3_f32 v66, v66, v100, v101
	v_max3_f32 v66, v66, v102, v103
	v_max3_f32 v66, v66, v104, v105
	v_mfma_f32_32x32x16_bf16 v[16:31], v[70:73], v[122:125], v[16:31]
	v_max3_f32 v66, v66, v106, v107
	v_max3_f32 v66, v66, v108, v109
	v_max3_f32 v66, v66, v110, v111
	v_max3_f32 v66, v66, v80, v81
	v_max3_f32 v66, v66, v82, v83
	v_max3_f32 v66, v66, v84, v85
	v_max3_f32 v66, v66, v86, v87
	v_mfma_f32_32x32x16_bf16 v[16:31], v[74:77], v[126:129], v[16:31]
	v_max3_f32 v66, v66, v88, v89
	v_max3_f32 v66, v66, v90, v91
	v_max3_f32 v66, v66, v92, v93
	v_max3_f32 v66, v66, v94, v95
	v_mov_b32_e32 v67, v66
	s_nop 1
	v_permlane32_swap_b32_e32 v66, v67
	v_mfma_f32_32x32x16_bf16 v[16:31], v[114:117], v[130:133], v[16:31]
	v_max_f32_e32 v67, v67, v67
	v_max_f32_e32 v66, v66, v66
	v_max_f32_e32 v67, v66, v67
	v_cmp_eq_f32_e32 vcc, 0, v164
	v_cmp_ge_f32_e64 s[40:41], s75, v67
	s_and_b64 s[0:1], vcc, s[40:41]
	v_cndmask_b32_e64 v66, 0, 1, s[0:1]
	v_cmp_ne_u32_e32 vcc, 0, v66
	s_cmp_eq_u64 vcc, exec
	v_mov_b32_e32 v66, 1.0
	s_cbranch_scc0 .LBB0_815
	v_cmp_gt_f32_e32 vcc, 1.0, v66
	s_cbranch_vccz .LBB0_808
